# P1: out-proj epilogue - all 16 residual pieces of a tile touched by early loads at the head of the epilogue so the per-piece serial loads hit cache; on top of C1+G1+B1+E2c+E8b
# speedup vs baseline: 1.0004x; 1.0004x over previous
.LBB0_1005:
	s_ashr_i32 s4, s44, 31
	s_lshr_b32 s4, s4, 20
	s_add_i32 s4, s44, s4
	s_ashr_i32 s4, s4, 12
	s_mul_hi_i32 s5, s4, 0xc000
	s_mul_i32 s4, s4, 0xc000
	v_lshl_or_b32 v166, s45, 8, v182
	s_add_u32 s4, s38, s4
	s_addc_u32 s5, s39, s5
	v_ashrrev_i32_e32 v167, 31, v166
	v_lshl_add_u64 v[76:77], v[166:167], 2, s[4:5]
	global_load_dwordx4 v[80:83], v[76:77], off offset:16
	global_load_dwordx4 v[84:87], v[76:77], off
	global_load_dwordx4 v[68:71], v[76:77], off offset:528
	s_nop 0
	global_load_dwordx4 v[76:79], v[76:77], off offset:512
	v_add_u32_e32 v172, s44, v180
	v_ashrrev_i32_e32 v173, 31, v172
	v_lshlrev_b64 v[144:145], 11, v[172:173]
	v_lshl_add_u64 v[178:179], v[144:145], 0, v[166:167]
	v_mov_b32_e32 v212, v178
	v_mov_b32_e32 v213, v179
	s_mov_b64 s[98:99], 0x8000
	s_cmp_lg_u64 s[8:9], 0
	s_cbranch_scc0 .LP1_f32
	v_lshl_add_u64 v[214:215], v[212:213], 1, s[10:11]
	global_load_dwordx4 v[208:211], v[214:215], off
	global_load_dwordx4 v[208:211], v[214:215], off offset:256
	v_lshl_add_u64 v[212:213], v[212:213], 0, s[98:99]
	v_lshl_add_u64 v[214:215], v[212:213], 1, s[10:11]
	global_load_dwordx4 v[208:211], v[214:215], off
	global_load_dwordx4 v[208:211], v[214:215], off offset:256
	v_lshl_add_u64 v[212:213], v[212:213], 0, s[98:99]
	v_lshl_add_u64 v[214:215], v[212:213], 1, s[10:11]
	global_load_dwordx4 v[208:211], v[214:215], off
	global_load_dwordx4 v[208:211], v[214:215], off offset:256
	v_lshl_add_u64 v[212:213], v[212:213], 0, s[98:99]
	v_lshl_add_u64 v[214:215], v[212:213], 1, s[10:11]
	global_load_dwordx4 v[208:211], v[214:215], off
	global_load_dwordx4 v[208:211], v[214:215], off offset:256
	s_mov_b64 s[98:99], 0x28000
	v_lshl_add_u64 v[212:213], v[212:213], 0, s[98:99]
	s_mov_b64 s[98:99], 0x8000
	v_lshl_add_u64 v[214:215], v[212:213], 1, s[10:11]
	global_load_dwordx4 v[208:211], v[214:215], off
	global_load_dwordx4 v[208:211], v[214:215], off offset:256
	v_lshl_add_u64 v[212:213], v[212:213], 0, s[98:99]
	v_lshl_add_u64 v[214:215], v[212:213], 1, s[10:11]
	global_load_dwordx4 v[208:211], v[214:215], off
	global_load_dwordx4 v[208:211], v[214:215], off offset:256
	v_lshl_add_u64 v[212:213], v[212:213], 0, s[98:99]
	v_lshl_add_u64 v[214:215], v[212:213], 1, s[10:11]
	global_load_dwordx4 v[208:211], v[214:215], off
	global_load_dwordx4 v[208:211], v[214:215], off offset:256
	v_lshl_add_u64 v[212:213], v[212:213], 0, s[98:99]
	v_lshl_add_u64 v[214:215], v[212:213], 1, s[10:11]
	global_load_dwordx4 v[208:211], v[214:215], off
	global_load_dwordx4 v[208:211], v[214:215], off offset:256
	s_branch .LP1_done
.LP1_f32:
	v_lshl_add_u64 v[214:215], v[212:213], 2, s[6:7]
	global_load_dwordx4 v[208:211], v[214:215], off
	global_load_dwordx4 v[208:211], v[214:215], off offset:16
	global_load_dwordx4 v[208:211], v[214:215], off offset:512
	global_load_dwordx4 v[208:211], v[214:215], off offset:528
	v_lshl_add_u64 v[212:213], v[212:213], 0, s[98:99]
	v_lshl_add_u64 v[214:215], v[212:213], 2, s[6:7]
	global_load_dwordx4 v[208:211], v[214:215], off
	global_load_dwordx4 v[208:211], v[214:215], off offset:16
	global_load_dwordx4 v[208:211], v[214:215], off offset:512
	global_load_dwordx4 v[208:211], v[214:215], off offset:528
	v_lshl_add_u64 v[212:213], v[212:213], 0, s[98:99]
	v_lshl_add_u64 v[214:215], v[212:213], 2, s[6:7]
	global_load_dwordx4 v[208:211], v[214:215], off
	global_load_dwordx4 v[208:211], v[214:215], off offset:16
	global_load_dwordx4 v[208:211], v[214:215], off offset:512
	global_load_dwordx4 v[208:211], v[214:215], off offset:528
	v_lshl_add_u64 v[212:213], v[212:213], 0, s[98:99]
	v_lshl_add_u64 v[214:215], v[212:213], 2, s[6:7]
	global_load_dwordx4 v[208:211], v[214:215], off
	global_load_dwordx4 v[208:211], v[214:215], off offset:16
	global_load_dwordx4 v[208:211], v[214:215], off offset:512
	global_load_dwordx4 v[208:211], v[214:215], off offset:528
	s_mov_b64 s[98:99], 0x28000
	v_lshl_add_u64 v[212:213], v[212:213], 0, s[98:99]
	s_mov_b64 s[98:99], 0x8000
	v_lshl_add_u64 v[214:215], v[212:213], 2, s[6:7]
	global_load_dwordx4 v[208:211], v[214:215], off
	global_load_dwordx4 v[208:211], v[214:215], off offset:16
	global_load_dwordx4 v[208:211], v[214:215], off offset:512
	global_load_dwordx4 v[208:211], v[214:215], off offset:528
	v_lshl_add_u64 v[212:213], v[212:213], 0, s[98:99]
	v_lshl_add_u64 v[214:215], v[212:213], 2, s[6:7]
	global_load_dwordx4 v[208:211], v[214:215], off
	global_load_dwordx4 v[208:211], v[214:215], off offset:16
	global_load_dwordx4 v[208:211], v[214:215], off offset:512
	global_load_dwordx4 v[208:211], v[214:215], off offset:528
	v_lshl_add_u64 v[212:213], v[212:213], 0, s[98:99]
	v_lshl_add_u64 v[214:215], v[212:213], 2, s[6:7]
	global_load_dwordx4 v[208:211], v[214:215], off
	global_load_dwordx4 v[208:211], v[214:215], off offset:16
	global_load_dwordx4 v[208:211], v[214:215], off offset:512
	global_load_dwordx4 v[208:211], v[214:215], off offset:528
	v_lshl_add_u64 v[212:213], v[212:213], 0, s[98:99]
	v_lshl_add_u64 v[214:215], v[212:213], 2, s[6:7]
	global_load_dwordx4 v[208:211], v[214:215], off
	global_load_dwordx4 v[208:211], v[214:215], off offset:16
	global_load_dwordx4 v[208:211], v[214:215], off offset:512
	global_load_dwordx4 v[208:211], v[214:215], off offset:528
.LP1_done:
	v_cndmask_b32_e64 v144, 0, 1, s[8:9]
	v_cmp_ne_u32_e64 s[4:5], 1, v144
	s_andn2_b64 vcc, exec, s[8:9]
	v_lshl_add_u64 v[176:177], v[178:179], 1, s[10:11]
	s_cbranch_vccnz .LBB0_1056
	global_load_dwordx4 v[144:147], v[176:177], off
	s_waitcnt vmcnt(0)
	v_lshlrev_b32_e32 v148, 16, v144
	v_and_b32_e32 v149, 0xffff0000, v144
	v_lshlrev_b32_e32 v150, 16, v145
	v_and_b32_e32 v151, 0xffff0000, v145
	v_lshlrev_b32_e32 v144, 16, v146
	v_and_b32_e32 v145, 0xffff0000, v146
	v_lshlrev_b32_e32 v146, 16, v147
	v_and_b32_e32 v147, 0xffff0000, v147
	v_lshl_add_u64 v[174:175], v[178:179], 2, s[6:7]
	s_cbranch_execnz .LBB0_1008
